# waitcnt placement: removed the compiler's conservative vmcnt(0) after the chunk-item flag store (it only stalled wave 0 on the store ack)
# baseline (speedup 1.0000x reference)
; #define GL_REPF(k) for (int rr_ = 0; rr_ < ((GL_REP_STEP == (k)) ? 2 : 1); ++rr_)
; #define GL_BAR() do { asm volatile("s_waitcnt lgkmcnt(0)" ::: "memory"); __builtin_amdgcn_s_barrier(); asm volatile("" ::: "memory"); } while (0)
; __device__ __forceinline__ void gdn_local_item(const Params& P, LAS unsigned char* lds, int item, int tid, bool defer, int& pend, unsigned& pend_fb) {
;     ...
;     if (pend >= 0) asm volatile("s_waitcnt vmcnt(0)" ::: "memory");
;     GL_BAR();
;     if (pend >= 0) { if (tid == 0) __hip_atomic_store((unsigned*)(ws + WS_CTL) + CW_GFLAG + pend, pend_fb, __ATOMIC_RELAXED, __HIP_MEMORY_SCOPE_AGENT); pend = -1; }
;     GL_REPF(1) {
;         const int c = tid >> 3, grp = tid & 7;
; #pragma unroll 1
;         for (int part = 0; part < 3; ++part) {
.LBB0_517:
	v_ashrrev_i32_e32 v92, 3, v91
	v_and_b32_e32 v46, 7, v91
	s_movk_i32 s0, 0x300
	v_lshlrev_b32_e32 v51, 6, v46
	v_lshlrev_b32_e32 v52, 5, v46
	s_nop 0
	s_mul_i32 s98, s58, 0xe0
	v_readlane_b32 s99, v255, 10
	s_add_i32 s98, s98, s99
	s_addk_i32 s98, 0xe0
	s_lshr_b32 s99, s98, 3
	s_cmpk_gt_u32 s99, 0x7f
	s_cbranch_scc1 .Lpf_skipA
	s_and_b32 s98, s98, 7
	s_lshr_b32 s100, s98, 2
	s_and_b32 s98, s98, 3
	s_lshl_b32 s100, s100, 13
	s_lshl_b32 s99, s99, 6
	s_add_i32 s99, s99, s100
	s_add_i32 s99, s99, -3
	s_mul_i32 s99, s99, 0xc00
	s_lshl_b32 s98, s98, 8
	s_add_u32 s98, s99, s98
	s_add_u32 s100, s24, 0x3c00000
	s_addc_u32 s101, s25, 0
	s_add_u32 s100, s100, s98
	s_addc_u32 s101, s101, 0
	s_mov_b32 s98, 0x2aaaaaab
	v_mul_hi_u32 v250, v0, s98
	v_mul_u32_u24_e32 v251, 6, v250
	v_sub_u32_e32 v251, v0, v251
	v_lshrrev_b32_e32 v252, 1, v251
	v_and_b32_e32 v251, 1, v251
	v_mul_u32_u24_e32 v250, 0xc00, v250
	v_lshl_add_u32 v250, v252, 10, v250
	v_lshl_add_u32 v250, v251, 7, v250
	v_mov_b32_e32 v251, 0x192
	v_cmp_gt_u32_e64 s[98:99], v251, v0
	s_mov_b64 exec, s[98:99]
	global_load_dword v253, v250, s[100:101]
	s_mov_b64 exec, -1

; #define GL_REPF(k) for (int rr_ = 0; rr_ < ((GL_REP_STEP == (k)) ? 2 : 1); ++rr_)
; #define GL_BAR() do { asm volatile("s_waitcnt lgkmcnt(0)" ::: "memory"); __builtin_amdgcn_s_barrier(); asm volatile("" ::: "memory"); } while (0)
; __device__ __forceinline__ void gdn_local_item(const Params& P, LAS unsigned char* lds, int item, int tid, bool defer, int& pend, unsigned& pend_fb) {
;     ...
;     if (pend >= 0) asm volatile("s_waitcnt vmcnt(0)" ::: "memory");
;     GL_BAR();
;     if (pend >= 0) { if (tid == 0) __hip_atomic_store((unsigned*)(ws + WS_CTL) + CW_GFLAG + pend, pend_fb, __ATOMIC_RELAXED, __HIP_MEMORY_SCOPE_AGENT); pend = -1; }
;     GL_REPF(1) {
;         const int c = tid >> 3, grp = tid & 7;
; #pragma unroll 1
;         for (int part = 0; part < 3; ++part) {
.LBB0_803:
	s_or_b64 exec, exec, s[0:1]
	v_ashrrev_i32_e32 v85, 3, v84
	s_movk_i32 s0, 0x210
	v_mul_lo_u32 v1, v85, s0
	s_movk_i32 s0, 0x110
	v_and_b32_e32 v45, 7, v84
	v_mul_lo_u32 v46, v85, s0
	s_movk_i32 s0, 0x300
	v_lshlrev_b32_e32 v49, 6, v45
	v_lshlrev_b32_e32 v50, 5, v45
	s_nop 0
	v_readlane_b32 s98, v255, 10
	s_addk_i32 s98, 0x360
	s_lshr_b32 s99, s98, 3
	s_cmpk_gt_u32 s99, 0x7f
	s_cbranch_scc1 .Lpf_skipB
	s_and_b32 s98, s98, 7
	s_lshr_b32 s100, s98, 2
	s_and_b32 s98, s98, 3
	s_lshl_b32 s100, s100, 13
	s_lshl_b32 s99, s99, 6
	s_add_i32 s99, s99, s100
	s_add_i32 s99, s99, -3
	s_mul_i32 s99, s99, 0xc00
	s_lshl_b32 s98, s98, 8
	s_add_u32 s98, s99, s98
	s_add_u32 s100, s24, 0x3c00000
	s_addc_u32 s101, s25, 0
	s_add_u32 s100, s100, s98
	s_addc_u32 s101, s101, 0
	s_mov_b32 s98, 0x2aaaaaab
	v_mul_hi_u32 v250, v0, s98
	v_mul_u32_u24_e32 v251, 6, v250
	v_sub_u32_e32 v251, v0, v251
	v_lshrrev_b32_e32 v252, 1, v251
	v_and_b32_e32 v251, 1, v251
	v_mul_u32_u24_e32 v250, 0xc00, v250
	v_lshl_add_u32 v250, v252, 10, v250
	v_lshl_add_u32 v250, v251, 7, v250
	v_mov_b32_e32 v251, 0x192
	v_cmp_gt_u32_e64 s[98:99], v251, v0
	s_mov_b64 exec, s[98:99]
	global_load_dword v253, v250, s[100:101]
	s_mov_b64 exec, -1

; #define GL_REPF(k) for (int rr_ = 0; rr_ < ((GL_REP_STEP == (k)) ? 2 : 1); ++rr_)
; #define GL_BAR() do { asm volatile("s_waitcnt lgkmcnt(0)" ::: "memory"); __builtin_amdgcn_s_barrier(); asm volatile("" ::: "memory"); } while (0)
; __device__ __forceinline__ void gdn_local_item(const Params& P, LAS unsigned char* lds, int item, int tid, bool defer, int& pend, unsigned& pend_fb) {
;     ...
;     if (pend >= 0) asm volatile("s_waitcnt vmcnt(0)" ::: "memory");
;     GL_BAR();
;     if (pend >= 0) { if (tid == 0) __hip_atomic_store((unsigned*)(ws + WS_CTL) + CW_GFLAG + pend, pend_fb, __ATOMIC_RELAXED, __HIP_MEMORY_SCOPE_AGENT); pend = -1; }
;     GL_REPF(1) {
;         const int c = tid >> 3, grp = tid & 7;
; #pragma unroll 1
;         for (int part = 0; part < 3; ++part) {
.LBB0_1085:
	s_or_b64 exec, exec, s[0:1]
	v_ashrrev_i32_e32 v85, 3, v84
	s_movk_i32 s0, 0x210
	v_mul_lo_u32 v1, v85, s0
	s_movk_i32 s0, 0x110
	v_and_b32_e32 v45, 7, v84
	v_mul_lo_u32 v46, v85, s0
	s_movk_i32 s0, 0x300
	v_lshlrev_b32_e32 v49, 6, v45
	v_lshlrev_b32_e32 v50, 5, v45
	s_nop 0
	v_mul_lo_u32 v2, v85, s0
	v_readlane_b32 s88, v254, 58
	v_or_b32_e32 v51, v2, v50
	s_mov_b32 s13, 0xffff0000
	s_mov_b32 s14, 0x800000
	s_mov_b32 s15, 0x14c00
	s_movk_i32 s16, 0x7fff
	v_mov_b32_e32 v52, 0x3db504f3
	v_mov_b32_e32 v53, v49
	v_readlane_b32 s89, v254, 59
	v_readlane_b32 s90, v254, 60
	v_readlane_b32 s91, v254, 61
	v_readlane_b32 s94, v255, 0
	v_readlane_b32 s95, v255, 1
	v_readlane_b32 s92, v254, 62
	v_readlane_b32 s93, v254, 63
	s_branch .LBB0_1087
